# speedup vs baseline: 1.0010x; 1.0010x over previous
.LBB7_6:
	s_or_b64 exec, exec, s[16:17]
	s_xor_b32 s7, s7, s20
	s_mul_i32 s20, s22, s18
	s_sub_i32 s20, s21, s20
	s_add_i32 s21, s22, 1
	s_sub_i32 s24, s20, s18
	s_cmp_ge_u32 s20, s18
	s_cselect_b32 s21, s21, s22
	s_cselect_b32 s20, s24, s20
	s_add_i32 s22, s21, 1
	s_cmp_ge_u32 s20, s18
	s_cselect_b32 s18, s22, s21
	s_xor_b32 s18, s18, s7
	s_sub_i32 s7, s18, s7
	s_load_dwordx2 s[16:17], s[0:1], 0x10
	s_load_dword s23, s[0:1], 0x28
	s_mul_i32 s3, s7, s3
	s_sub_i32 s3, s19, s3
	v_lshlrev_b32_e32 v2, 3, v0
	s_mul_i32 s18, s7, s5
	s_lshl_b32 s3, s3, 6
	v_lshrrev_b32_e32 v32, 2, v0
	v_and_b32_e32 v10, 24, v2
	s_ashr_i32 s19, s18, 31
	v_or_b32_e32 v6, s3, v32
	s_ashr_i32 s7, s3, 31
	v_lshl_add_u64 v[2:3], s[18:19], 0, v[10:11]
	s_waitcnt lgkmcnt(0)
	s_mul_i32 s7, s16, s7
	v_mad_u64_u32 v[4:5], s[18:19], s16, v6, v[2:3]
	v_mul_lo_u32 v6, s17, v6
	v_add3_u32 v5, v6, v5, s7
	v_add_u32_e32 v6, s2, v32
	s_add_i32 s7, s4, -1
	v_min_i32_e32 v6, s7, v6
	v_mad_i64_i32 v[6:7], s[16:17], v6, s23, v[2:3]
	v_lshlrev_b64 v[6:7], 1, v[6:7]
	v_lshlrev_b64 v[8:9], 1, v[4:5]
	v_lshl_add_u64 v[4:5], s[12:13], 0, v[6:7]
	global_load_dwordx4 v[70:73], v[4:5], off
	v_lshl_add_u64 v[6:7], s[14:15], 0, v[6:7]
	v_lshl_add_u64 v[2:3], s[8:9], 0, v[8:9]
	global_load_dwordx4 v[74:77], v[6:7], off
	global_load_dwordx4 v[78:81], v[2:3], off
	v_lshl_add_u64 v[8:9], s[10:11], 0, v[8:9]
	global_load_dwordx4 v[82:85], v[8:9], off
	s_load_dwordx2 s[8:9], s[0:1], 0x38
	v_and_b32_e32 v11, 32, v32
	v_mul_u32_u24_e32 v32, 40, v32
	v_lshlrev_b32_e32 v10, 1, v10
	v_bfe_u32 v14, v0, 5, 1
	v_lshl_add_u32 v10, v32, 1, v10
	s_ashr_i32 s7, s5, 31
	s_lshr_b32 s7, s7, 27
	s_add_i32 s5, s5, s7
	s_ashr_i32 s5, s5, 5
	s_add_i32 s7, s5, -1
	s_min_i32 s10, s7, 2
	s_lshl_b32 s10, s10, 5
	s_ashr_i32 s11, s10, 31
	s_lshl_b64 s[10:11], s[10:11], 1
	v_lshl_add_u64 v[16:17], v[2:3], 0, s[10:11]
	global_load_dwordx4 v[18:21], v[2:3], off offset:64
	global_load_dwordx4 v[22:25], v[8:9], off offset:64
	global_load_dwordx4 v[26:29], v[4:5], off offset:64
	global_load_dwordx4 v[34:37], v[6:7], off offset:64
	global_load_dwordx4 v[30:33], v[16:17], off
	v_lshl_add_u64 v[16:17], v[8:9], 0, s[10:11]
	global_load_dwordx4 v[38:41], v[16:17], off
	v_lshl_add_u64 v[16:17], v[4:5], 0, s[10:11]
	global_load_dwordx4 v[42:45], v[16:17], off
	v_lshl_add_u64 v[16:17], v[6:7], 0, s[10:11]
	global_load_dwordx4 v[46:49], v[16:17], off
	s_waitcnt vmcnt(11)
	ds_write_b128 v10, v[70:73] offset:10240
	s_waitcnt vmcnt(10)
	ds_write_b128 v10, v[74:77] offset:15360
	s_waitcnt vmcnt(9)
	ds_write_b128 v10, v[78:81]
	s_waitcnt vmcnt(8)
	ds_write_b128 v10, v[82:85] offset:5120
	s_waitcnt lgkmcnt(0)
	s_barrier
	v_lshlrev_b32_e32 v17, 4, v14
	s_movk_i32 s10, 0x50
	v_or_b32_e32 v16, v11, v12
	v_mul_u32_u24_e32 v66, 0x50, v15
	v_mad_u32_u24 v15, v15, s10, v17
	v_mul_u32_u24_e32 v67, 0x50, v16
	v_mad_u32_u24 v16, v16, s10, v17
	ds_read_b128 v[58:61], v15 offset:15360
	ds_read_b128 v[50:53], v15 offset:10240
	ds_read_b128 v[54:57], v16
	ds_read_b128 v[62:65], v16 offset:5120
	v_accvgpr_write_b32 a15, 0
	v_accvgpr_write_b32 a14, 0
	v_accvgpr_write_b32 a13, 0
	v_accvgpr_write_b32 a12, 0
	v_accvgpr_write_b32 a11, 0
	v_accvgpr_write_b32 a10, 0
	v_accvgpr_write_b32 a9, 0
	v_accvgpr_write_b32 a8, 0
	v_accvgpr_write_b32 a7, 0
	v_accvgpr_write_b32 a6, 0
	v_accvgpr_write_b32 a5, 0
	v_accvgpr_write_b32 a4, 0
	v_accvgpr_write_b32 a3, 0
	v_accvgpr_write_b32 a2, 0
	v_accvgpr_write_b32 a1, 0
	v_accvgpr_write_b32 a0, 0
	s_mov_b32 s10, 0
	v_add_u32_e32 v15, v17, v67
	v_add_u32_e32 v16, v17, v66

.LBB7_9:
	v_lshrrev_b32_e32 v3, 6, v0
	v_mul_u32_u24_e32 v3, 0x1200, v3
	s_waitcnt vmcnt(6)
	s_nop 5
	v_accvgpr_read_b32 v23, a0
	v_accvgpr_read_b32 v22, a1
	v_lshl_or_b32 v12, v12, 2, v3
	s_movk_i32 s5, 0x240
	v_accvgpr_read_b32 v21, a2
	v_accvgpr_read_b32 v20, a3
	v_fma_f32 v23, s6, v23, v13
	v_mad_u32_u24 v12, v14, s5, v12
	v_fma_f32 v14, s6, v22, v13
	v_accvgpr_read_b32 v19, a4
	v_accvgpr_read_b32 v18, a5
	s_waitcnt lgkmcnt(0)
	s_barrier
	ds_write2_b32 v12, v23, v14 offset1:36
	v_fma_f32 v14, s6, v21, v13
	v_fma_f32 v20, s6, v20, v13
	v_and_b32_e32 v2, 63, v0
	v_accvgpr_read_b32 v17, a6
	v_accvgpr_read_b32 v16, a7
	ds_write2_b32 v12, v14, v20 offset0:72 offset1:108
	v_fma_f32 v14, s6, v19, v13
	v_fma_f32 v18, s6, v18, v13
	v_add_u32_e32 v19, 0x400, v12
	v_lshlrev_b32_e32 v0, 2, v0
	v_accvgpr_read_b32 v15, a8
	v_accvgpr_read_b32 v10, a9
	v_accvgpr_read_b32 v9, a10
	v_accvgpr_read_b32 v8, a11
	v_accvgpr_read_b32 v7, a12
	v_accvgpr_read_b32 v6, a13
	v_accvgpr_read_b32 v5, a14
	v_accvgpr_read_b32 v4, a15
	ds_write2_b32 v19, v14, v18 offset0:32 offset1:68
	v_fma_f32 v14, s6, v17, v13
	v_fma_f32 v16, s6, v16, v13
	v_and_b32_e32 v0, 28, v0
	ds_write2_b32 v19, v14, v16 offset0:104 offset1:140
	v_fma_f32 v14, s6, v15, v13
	v_fma_f32 v10, s6, v10, v13
	v_add_u32_e32 v15, 0x800, v12
	v_fma_f32 v9, s6, v9, v13
	v_fma_f32 v8, s6, v8, v13
	v_fma_f32 v7, s6, v7, v13
	v_fma_f32 v6, s6, v6, v13
	v_fma_f32 v5, s6, v5, v13
	v_fmac_f32_e32 v13, s6, v4
	v_or3_b32 v4, s2, v1, v0
	ds_write2_b32 v15, v9, v8 offset0:136 offset1:172
	v_add_u32_e32 v8, 0xc00, v12
	v_cmp_gt_i32_e32 vcc, s4, v4
	ds_write2_b32 v15, v14, v10 offset0:64 offset1:100
	ds_write2_b32 v8, v7, v6 offset0:96 offset1:132
	ds_write2_b32 v8, v5, v13 offset0:168 offset1:204
	s_and_saveexec_b64 s[4:5], vcc
	s_cbranch_execz .LBB7_11
	s_load_dwordx2 s[0:1], s[0:1], 0x40
	v_add_u32_e32 v4, s3, v11
	v_ashrrev_i32_e32 v5, 31, v4
	s_ashr_i32 s3, s2, 31
	v_lshlrev_b32_e32 v0, 2, v0
	s_waitcnt lgkmcnt(0)
	v_mul_lo_u32 v6, s0, v5
	v_mul_lo_u32 v7, s1, v4
	v_mad_u64_u32 v[4:5], s[4:5], s0, v4, 0
	v_add3_u32 v5, v5, v6, v7
	v_lshl_add_u64 v[4:5], v[4:5], 2, s[8:9]
	v_lshl_add_u64 v[4:5], s[2:3], 2, v[4:5]
	v_lshlrev_b32_e32 v6, 2, v1
	v_mov_b32_e32 v7, 0
	v_lshl_add_u64 v[4:5], v[4:5], 0, v[6:7]
	v_mov_b32_e32 v1, v7
	v_lshrrev_b32_e32 v12, 3, v2
	v_lshl_add_u64 v[8:9], v[4:5], 0, v[0:1]
	v_mul_u32_u24_e32 v1, 0x90, v12
	v_add3_u32 v13, v3, v0, v1
	ds_read_b128 v[0:3], v13
	v_mad_u64_u32 v[4:5], s[2:3], s0, v12, 0
	v_mov_b32_e32 v6, v5
	v_mad_u64_u32 v[6:7], s[2:3], s1, v12, v[6:7]
	v_mov_b32_e32 v5, v6
	v_lshl_add_u64 v[10:11], v[4:5], 2, v[8:9]
	ds_read_b128 v[4:7], v13 offset:1152
	s_waitcnt lgkmcnt(1)
	global_store_dwordx4 v[10:11], v[0:3], off sc1
	s_nop 1
	v_or_b32_e32 v3, 8, v12
	v_mad_u64_u32 v[0:1], s[2:3], s0, v3, 0
	v_mov_b32_e32 v2, v1
	v_mad_u64_u32 v[2:3], s[2:3], s1, v3, v[2:3]
	v_mov_b32_e32 v1, v2
	v_lshl_add_u64 v[0:1], v[0:1], 2, v[8:9]
	s_waitcnt lgkmcnt(0)
	global_store_dwordx4 v[0:1], v[4:7], off sc1
	ds_read_b128 v[0:3], v13 offset:2304
	s_nop 0
	v_or_b32_e32 v7, 16, v12
	v_mad_u64_u32 v[4:5], s[2:3], s0, v7, 0
	v_mov_b32_e32 v6, v5
	v_mad_u64_u32 v[6:7], s[2:3], s1, v7, v[6:7]
	v_mov_b32_e32 v5, v6
	v_lshl_add_u64 v[10:11], v[4:5], 2, v[8:9]
	ds_read_b128 v[4:7], v13 offset:3456
	s_waitcnt lgkmcnt(1)
	global_store_dwordx4 v[10:11], v[0:3], off sc1
	s_nop 1
	v_or_b32_e32 v3, 24, v12
	v_mad_u64_u32 v[0:1], s[2:3], s0, v3, 0
	v_mov_b32_e32 v2, v1
	v_mad_u64_u32 v[2:3], s[0:1], s1, v3, v[2:3]
	v_mov_b32_e32 v1, v2
	v_lshl_add_u64 v[0:1], v[0:1], 2, v[8:9]
	s_waitcnt lgkmcnt(0)
	global_store_dwordx4 v[0:1], v[4:7], off sc1
.LBB7_11:
	s_endpgm
	s_endpgm
	s_endpgm
	s_endpgm
	s_endpgm
	s_endpgm
	s_endpgm
	s_endpgm
	s_endpgm
	s_endpgm
	s_endpgm
	s_endpgm
	s_endpgm
	s_endpgm
	s_endpgm
	s_endpgm
	s_endpgm
	s_endpgm
	s_endpgm

.LBB18_6:
	s_or_b64 exec, exec, s[2:3]
	s_xor_b32 s2, s20, s19
	s_mul_i32 s19, s22, s17
	s_sub_i32 s19, s21, s19
	s_add_i32 s20, s22, 1
	s_sub_i32 s21, s19, s17
	s_cmp_ge_u32 s19, s17
	s_cselect_b32 s20, s20, s22
	s_cselect_b32 s19, s21, s19
	s_add_i32 s21, s20, 1
	s_cmp_ge_u32 s19, s17
	s_cselect_b32 s17, s21, s20
	s_xor_b32 s17, s17, s2
	s_sub_i32 s17, s17, s2
	s_load_dwordx2 s[24:25], s[0:1], 0x10
	s_load_dword s3, s[0:1], 0x28
	s_mul_i32 s2, s17, s16
	s_sub_i32 s2, s18, s2
	v_lshlrev_b32_e32 v2, 3, v0
	s_mul_i32 s16, s17, s5
	s_lshl_b32 s2, s2, 6
	v_lshrrev_b32_e32 v15, 2, v0
	v_and_b32_e32 v2, 24, v2
	s_ashr_i32 s17, s16, 31
	v_or_b32_e32 v8, s2, v15
	s_ashr_i32 s18, s2, 31
	v_lshl_add_u64 v[4:5], s[16:17], 0, v[2:3]
	s_waitcnt lgkmcnt(0)
	s_mul_i32 s18, s24, s18
	v_mad_u64_u32 v[6:7], s[16:17], s24, v8, v[4:5]
	v_mul_lo_u32 v3, s25, v8
	v_add3_u32 v7, v3, v7, s18
	v_add_u32_e32 v3, s7, v15
	s_add_i32 s4, s4, -1
	v_min_i32_e32 v3, s4, v3
	v_mad_i64_i32 v[8:9], s[16:17], v3, s3, v[4:5]
	v_lshlrev_b64 v[8:9], 1, v[8:9]
	v_lshlrev_b64 v[10:11], 1, v[6:7]
	v_lshl_add_u64 v[6:7], s[12:13], 0, v[8:9]
	global_load_dwordx4 v[70:73], v[6:7], off
	v_lshl_add_u64 v[8:9], s[14:15], 0, v[8:9]
	v_lshl_add_u64 v[4:5], s[8:9], 0, v[10:11]
	global_load_dwordx4 v[74:77], v[8:9], off
	global_load_dwordx4 v[78:81], v[4:5], off
	v_lshl_add_u64 v[10:11], s[10:11], 0, v[10:11]
	global_load_dwordx4 v[82:85], v[10:11], off
	v_and_b32_e32 v3, 32, v15
	v_mul_u32_u24_e32 v15, 40, v15
	v_lshlrev_b32_e32 v17, 1, v2
	v_bfe_u32 v14, v0, 5, 1
	v_lshl_add_u32 v15, v15, 1, v17
	s_ashr_i32 s3, s5, 31
	s_lshr_b32 s3, s3, 27
	s_add_i32 s3, s5, s3
	s_ashr_i32 s3, s3, 5
	s_add_i32 s4, s3, -1
	s_min_i32 s5, s4, 2
	s_lshl_b32 s8, s5, 5
	s_ashr_i32 s9, s8, 31
	global_load_dwordx4 v[18:21], v[4:5], off offset:64
	global_load_dwordx4 v[22:25], v[10:11], off offset:64
	global_load_dwordx4 v[26:29], v[6:7], off offset:64
	global_load_dwordx4 v[34:37], v[8:9], off offset:64
	s_lshl_b64 s[8:9], s[8:9], 1
	v_lshl_add_u64 v[30:31], v[4:5], 0, s[8:9]
	v_lshl_add_u64 v[38:39], v[10:11], 0, s[8:9]
	v_lshl_add_u64 v[42:43], v[6:7], 0, s[8:9]
	v_lshl_add_u64 v[46:47], v[8:9], 0, s[8:9]
	global_load_dwordx4 v[30:33], v[30:31], off
	v_lshlrev_b32_e32 v66, 4, v14
	global_load_dwordx4 v[38:41], v[38:39], off
	s_movk_i32 s5, 0x50
	global_load_dwordx4 v[42:45], v[42:43], off
	v_or_b32_e32 v17, v3, v13
	global_load_dwordx4 v[46:49], v[46:47], off
	s_waitcnt vmcnt(11)
	ds_write_b128 v15, v[70:73] offset:10240
	s_waitcnt vmcnt(10)
	ds_write_b128 v15, v[74:77] offset:15360
	s_waitcnt vmcnt(9)
	ds_write_b128 v15, v[78:81]
	s_waitcnt vmcnt(8)
	ds_write_b128 v15, v[82:85] offset:5120
	s_waitcnt lgkmcnt(0)
	s_barrier
	v_mul_u32_u24_e32 v67, 0x50, v16
	v_mad_u32_u24 v16, v16, s5, v66
	v_mul_u32_u24_e32 v68, 0x50, v17
	v_mad_u32_u24 v17, v17, s5, v66
	ds_read_b128 v[58:61], v16 offset:15360
	ds_read_b128 v[50:53], v16 offset:10240
	ds_read_b128 v[54:57], v17
	ds_read_b128 v[62:65], v17 offset:5120
	v_accvgpr_write_b32 a15, 0
	v_accvgpr_write_b32 a14, 0
	v_accvgpr_write_b32 a13, 0
	v_accvgpr_write_b32 a12, 0
	v_accvgpr_write_b32 a11, 0
	v_accvgpr_write_b32 a10, 0
	v_accvgpr_write_b32 a9, 0
	v_accvgpr_write_b32 a8, 0
	v_accvgpr_write_b32 a7, 0
	v_accvgpr_write_b32 a6, 0
	v_accvgpr_write_b32 a5, 0
	v_accvgpr_write_b32 a4, 0
	v_accvgpr_write_b32 a3, 0
	v_accvgpr_write_b32 a2, 0
	v_accvgpr_write_b32 a1, 0
	v_accvgpr_write_b32 a0, 0
	s_mov_b32 s5, 0
	v_add_u32_e32 v16, v66, v68
	v_add_u32_e32 v17, v66, v67

.LBB18_9:
	s_waitcnt vmcnt(7)
	s_nop 7
	v_accvgpr_read_b32 v21, a1
	v_mul_u32_u24_e32 v14, 0xa0, v14
	s_waitcnt vmcnt(6)
	v_accvgpr_read_b32 v22, a0
	v_or_b32_e32 v13, v14, v13
	v_fma_f32 v14, s6, v21, v12
	v_lshrrev_b32_e32 v23, 6, v0
	v_fma_f32 v22, s6, v22, v12
	s_mov_b32 s3, 0x43800000
	v_max_f32_e32 v14, 0, v14
	v_mul_u32_u24_e32 v23, 0x1400, v23
	v_max_f32_e32 v22, 0, v22
	v_fma_mixlo_f16 v21, v14, s3, 0
	v_accvgpr_read_b32 v20, a2
	v_fma_mixlo_f16 v24, v22, s3, 0
	v_lshl_or_b32 v13, v13, 1, v23
	v_fma_mixlo_f16 v14, v14, s3, -v21 op_sel_hi:[0,0,1]
	s_load_dwordx4 s[8:11], s[0:1], 0x50
	v_fma_mixlo_f16 v22, v22, s3, -v24 op_sel_hi:[0,0,1]
	s_load_dwordx2 s[0:1], s[0:1], 0x40
	s_waitcnt lgkmcnt(0)
	s_barrier
	ds_write_b16 v13, v24
	ds_write_b16 v13, v22 offset:2560
	ds_write_b16 v13, v21 offset:80
	ds_write_b16 v13, v14 offset:2640
	v_fma_f32 v14, s6, v20, v12
	v_max_f32_e32 v14, 0, v14
	v_fma_mixlo_f16 v20, v14, s3, 0
	v_accvgpr_read_b32 v19, a3
	v_fma_mixlo_f16 v14, v14, s3, -v20 op_sel_hi:[0,0,1]
	ds_write_b16 v13, v20 offset:160
	ds_write_b16 v13, v14 offset:2720
	v_fma_f32 v14, s6, v19, v12
	v_max_f32_e32 v14, 0, v14
	v_fma_mixlo_f16 v19, v14, s3, 0
	v_accvgpr_read_b32 v18, a4
	v_fma_mixlo_f16 v14, v14, s3, -v19 op_sel_hi:[0,0,1]
	ds_write_b16 v13, v19 offset:240
	ds_write_b16 v13, v14 offset:2800
	v_fma_f32 v14, s6, v18, v12
	v_max_f32_e32 v14, 0, v14
	v_fma_mixlo_f16 v18, v14, s3, 0
	v_accvgpr_read_b32 v17, a5
	v_fma_mixlo_f16 v14, v14, s3, -v18 op_sel_hi:[0,0,1]
	ds_write_b16 v13, v18 offset:640
	ds_write_b16 v13, v14 offset:3200
	v_fma_f32 v14, s6, v17, v12
	v_max_f32_e32 v14, 0, v14
	v_fma_mixlo_f16 v17, v14, s3, 0
	v_accvgpr_read_b32 v16, a6
	v_fma_mixlo_f16 v14, v14, s3, -v17 op_sel_hi:[0,0,1]
	ds_write_b16 v13, v17 offset:720
	ds_write_b16 v13, v14 offset:3280
	v_fma_f32 v14, s6, v16, v12
	v_max_f32_e32 v14, 0, v14
	v_fma_mixlo_f16 v16, v14, s3, 0
	v_accvgpr_read_b32 v15, a7
	v_fma_mixlo_f16 v14, v14, s3, -v16 op_sel_hi:[0,0,1]
	ds_write_b16 v13, v16 offset:800
	ds_write_b16 v13, v14 offset:3360
	v_fma_f32 v14, s6, v15, v12
	v_accvgpr_read_b32 v11, a8
	v_max_f32_e32 v14, 0, v14
	v_fma_mixlo_f16 v15, v14, s3, 0
	v_fma_f32 v11, s6, v11, v12
	v_accvgpr_read_b32 v10, a9
	v_fma_mixlo_f16 v14, v14, s3, -v15 op_sel_hi:[0,0,1]
	v_max_f32_e32 v11, 0, v11
	ds_write_b16 v13, v15 offset:880
	ds_write_b16 v13, v14 offset:3440
	v_fma_mixlo_f16 v14, v11, s3, 0
	v_fma_f32 v10, s6, v10, v12
	v_accvgpr_read_b32 v9, a10
	v_fma_mixlo_f16 v11, v11, s3, -v14 op_sel_hi:[0,0,1]
	v_max_f32_e32 v10, 0, v10
	ds_write_b16 v13, v14 offset:1280
	ds_write_b16 v13, v11 offset:3840
	v_fma_mixlo_f16 v11, v10, s3, 0
	v_fma_f32 v9, s6, v9, v12
	v_accvgpr_read_b32 v8, a11
	v_fma_mixlo_f16 v10, v10, s3, -v11 op_sel_hi:[0,0,1]
	v_max_f32_e32 v9, 0, v9
	ds_write_b16 v13, v11 offset:1360
	ds_write_b16 v13, v10 offset:3920
	v_fma_mixlo_f16 v10, v9, s3, 0
	v_fma_f32 v8, s6, v8, v12
	v_accvgpr_read_b32 v7, a12
	v_fma_mixlo_f16 v9, v9, s3, -v10 op_sel_hi:[0,0,1]
	v_max_f32_e32 v8, 0, v8
	ds_write_b16 v13, v10 offset:1440
	ds_write_b16 v13, v9 offset:4000
	v_fma_mixlo_f16 v9, v8, s3, 0
	v_fma_f32 v7, s6, v7, v12
	v_accvgpr_read_b32 v6, a13
	v_fma_mixlo_f16 v8, v8, s3, -v9 op_sel_hi:[0,0,1]
	v_max_f32_e32 v7, 0, v7
	ds_write_b16 v13, v9 offset:1520
	ds_write_b16 v13, v8 offset:4080
	v_fma_mixlo_f16 v8, v7, s3, 0
	v_fma_f32 v6, s6, v6, v12
	v_accvgpr_read_b32 v5, a14
	v_fma_mixlo_f16 v7, v7, s3, -v8 op_sel_hi:[0,0,1]
	v_max_f32_e32 v6, 0, v6
	ds_write_b16 v13, v8 offset:1920
	ds_write_b16 v13, v7 offset:4480
	v_fma_mixlo_f16 v7, v6, s3, 0
	v_fma_f32 v5, s6, v5, v12
	v_accvgpr_read_b32 v4, a15
	v_fma_mixlo_f16 v6, v6, s3, -v7 op_sel_hi:[0,0,1]
	v_max_f32_e32 v5, 0, v5
	ds_write_b16 v13, v7 offset:2000
	ds_write_b16 v13, v6 offset:4560
	v_fma_mixlo_f16 v6, v5, s3, 0
	v_fmac_f32_e32 v12, s6, v4
	v_fma_mixlo_f16 v5, v5, s3, -v6 op_sel_hi:[0,0,1]
	v_max_f32_e32 v4, 0, v12
	ds_write_b16 v13, v6 offset:2080
	ds_write_b16 v13, v5 offset:4640
	v_fma_mixlo_f16 v5, v4, s3, 0
	v_and_b32_e32 v0, 63, v0
	v_fma_mixlo_f16 v4, v4, s3, -v5 op_sel_hi:[0,0,1]
	v_add_u32_e32 v3, s2, v3
	s_ashr_i32 s2, s7, 31
	ds_write_b16 v13, v5 offset:2160
	ds_write_b16 v13, v4 offset:4720
	v_lshrrev_b32_e32 v20, 2, v0
	v_ashrrev_i32_e32 v4, 31, v3
	v_or3_b32 v0, v1, v2, s7
	v_mov_b32_e32 v1, s2
	v_mul_lo_u32 v4, s0, v4
	v_mad_u64_u32 v[0:1], s[2:3], s0, v3, v[0:1]
	v_mul_lo_u32 v3, s1, v3
	v_add3_u32 v1, v3, v1, v4
	v_lshlrev_b64 v[0:1], 1, v[0:1]
	v_lshl_or_b32 v2, v2, 1, v23
	v_lshl_add_u64 v[12:13], s[8:9], 0, v[0:1]
	v_lshl_add_u64 v[14:15], s[10:11], 0, v[0:1]
	v_mul_u32_u24_e32 v0, 40, v20
	v_lshl_add_u32 v21, v0, 1, v2
	v_mad_u64_u32 v[8:9], s[2:3], s0, v20, 0
	ds_read_b128 v[0:3], v21
	ds_read_b128 v[4:7], v21 offset:2560
	v_mov_b32_e32 v10, v9
	v_mad_u64_u32 v[10:11], s[2:3], s1, v20, v[10:11]
	v_mov_b32_e32 v9, v10
	v_lshlrev_b64 v[16:17], 1, v[8:9]
	v_lshl_add_u64 v[18:19], v[12:13], 0, v[16:17]
	v_lshl_add_u64 v[16:17], v[14:15], 0, v[16:17]
	s_waitcnt lgkmcnt(0)
	global_store_dwordx4 v[16:17], v[4:7], off sc1
	ds_read_b128 v[8:11], v21 offset:1280
	global_store_dwordx4 v[18:19], v[0:3], off sc1
	v_or_b32_e32 v7, 16, v20
	v_mad_u64_u32 v[4:5], s[2:3], s0, v7, 0
	ds_read_b128 v[0:3], v21 offset:3840
	v_mov_b32_e32 v6, v5
	v_mad_u64_u32 v[6:7], s[0:1], s1, v7, v[6:7]
	v_mov_b32_e32 v5, v6
	v_lshlrev_b64 v[4:5], 1, v[4:5]
	v_lshl_add_u64 v[6:7], v[12:13], 0, v[4:5]
	v_lshl_add_u64 v[4:5], v[14:15], 0, v[4:5]
	s_waitcnt lgkmcnt(1)
	global_store_dwordx4 v[6:7], v[8:11], off sc1
	s_waitcnt lgkmcnt(0)
	global_store_dwordx4 v[4:5], v[0:3], off sc1
	s_endpgm
	s_endpgm
	s_endpgm
	s_endpgm
	s_endpgm
	s_endpgm
	s_endpgm
	s_endpgm
	s_endpgm
	s_endpgm
	s_endpgm
	s_endpgm
	s_endpgm
	s_endpgm
	s_endpgm
	s_endpgm
	s_endpgm
	s_endpgm
	s_endpgm
	s_endpgm
	s_endpgm
	s_endpgm
	s_endpgm
	s_endpgm
	s_endpgm
	s_endpgm
	s_endpgm
	s_endpgm
	s_endpgm
	s_endpgm
	s_endpgm
	s_endpgm
	s_endpgm
	s_endpgm
	s_endpgm
	s_endpgm
	s_endpgm
	s_endpgm
	s_endpgm
	s_endpgm
	s_endpgm
	s_endpgm
	s_endpgm
	s_endpgm
	s_endpgm
	s_endpgm
